# plus: P2 MMA-role steps use per-item precomputed causal bit-masks (v_and) instead of 32 recomputed compare instructions per step
# speedup vs baseline: 1.0320x; 1.0066x over previous
; #define LAS __attribute__((address_space(3)))
; #define LDS_WAIT() asm volatile("s_waitcnt lgkmcnt(0)" ::: "memory")
; DI void h_opsk_load(HOpsK& P, LAS unsigned char* buf, int kb, int r32, int hh) {
; #pragma unroll
;     for (int st = 0; st < 2; ++st) {
;         P.ka[st] = *(const LAS bf16x8*)(buf + H_KS + r32 * 272 + (kb * 32 + 16 * st + 8 * hh) * 2);
;         P.qb[st] = *(const LAS bf16x8*)(buf + H_QS + r32 * 272 + (kb * 32 + 16 * st + 8 * hh) * 2);
;         P.ku[st] = *(const LAS bf16x8*)(buf + H_KU + (kb * 32 + r32) * 80 + (16 * st + 8 * hh) * 2);
;         const LAS unsigned char* qp = buf + H_QS + r32 * 272 + (kb * 32 + 16 * st + 4 * hh) * 2;
;         const u32x2 q0 = *(const LAS u32x2*)qp, q1 = *(const LAS u32x2*)(qp + 16);
;         P.qq[st].x = q0.x; P.qq[st].y = q0.y; P.qq[st].z = q1.x; P.qq[st].w = q1.y;
;     }
; #pragma unroll
;     for (int g = 0; g < 4; ++g) { P.dec[g] = *(const LAS f32x4*)(buf + H_DEC + (kb * 32 + 8 * g + 4 * hh) * 4); P.ebm[g] = *(const LAS f32x4*)(buf + H_EBM + (kb * 32 + 8 * g + 4 * hh) * 4); }
; }
; DI void h_mma2(f32x16& S0, f32x16& S1, LAS unsigned char* buf, LAS unsigned char* red, int kbp, int vb, int r32, int hh) {
;     int rq = r32; asm volatile("" : "+v"(rq));
;     bf16x8 vt[2]; u32x4 vv[2];
; #pragma unroll
;     for (int st = 0; st < 2; ++st) {
;         vt[st] = *(const LAS bf16x8*)(buf + H_VT + (vb * 32 + r32) * 80 + (16 * st + 8 * hh) * 2);
;         const LAS unsigned char* vp = buf + H_VT + (vb * 32 + r32) * 80 + (16 * st + 4 * hh) * 2;
;         const u32x2 v0 = *(const LAS u32x2*)vp, v1 = *(const LAS u32x2*)(vp + 16);
;         vv[st].x = v0.x; vv[st].y = v0.y; vv[st].z = v1.x; vv[st].w = v1.y;
;     }
;     f32x16 Osum;
; #pragma unroll
;     for (int kk = 0; kk < 2; ++kk) {
;         HOpsK P; h_opsk_load(P, buf, 2 * kbp + kk, r32, hh);
;         f32x16& S = (kk == 0) ? S0 : S1; f32x16 O;
;         LDS_WAIT(); __builtin_amdgcn_sched_barrier(0);
.LBB0_413:
	s_and_b32 s4, s39, 1
	v_mov_b32_e32 v2, v0
	s_mul_i32 s5, s4, 0xb400
	s_add_i32 s62, s5, 0
	v_and_b32_e32 v193, 31, v2
	v_bfe_u32 v2, v2, 5, 1
	v_or_b32_e32 v5, s3, v193
	v_mov_b32_e32 v6, s62
	s_lshl_b32 s4, s4, 14
	v_lshlrev_b32_e32 v4, 8, v2
	v_mad_u32_u24 v5, v5, s86, v6
	v_lshlrev_b32_e32 v226, 4, v2
	v_lshlrev_b32_e32 v218, 3, v2
	s_add_i32 s4, s4, 0
	v_or3_b32 v4, v4, s73, v193
	v_add_u32_e32 v7, v5, v226
	v_add_u32_e32 v5, v5, v218
	v_lshl_add_u32 v242, v4, 2, s4
	v_mov_b32_e32 v4, v193
	v_add_u32_e32 v5, 0x8800, v5
	v_lshlrev_b32_e32 v2, 2, v2
	ds_read2_b64 v[100:103], v5 offset0:192 offset1:194
	ds_read2_b64 v[104:107], v5 offset0:196 offset1:198
	ds_read_b128 v[108:111], v7 offset:36352
	ds_read_b128 v[112:115], v7 offset:36384
	v_or_b32_e32 v5, 2, v2
	v_cmp_gt_i32_e64 s[6:7], v5, v4
	v_or_b32_e32 v5, 3, v2
	v_cmp_gt_i32_e64 s[8:9], v5, v4
	v_or_b32_e32 v5, 8, v2
	v_cmp_gt_i32_e64 s[10:11], v5, v4
	v_or_b32_e32 v5, 9, v2
	v_cmp_gt_i32_e64 s[12:13], v5, v4
	v_or_b32_e32 v5, 10, v2
	v_cmp_gt_i32_e64 s[14:15], v5, v4
	v_or_b32_e32 v5, 11, v2
	v_cmp_gt_i32_e64 s[16:17], v5, v4
	v_or_b32_e32 v5, 16, v2
	v_cmp_gt_i32_e64 s[18:19], v5, v4
	v_or_b32_e32 v5, 17, v2
	v_cmp_gt_i32_e64 s[20:21], v5, v4
	v_or_b32_e32 v5, 18, v2
	v_cmp_gt_i32_e64 s[22:23], v5, v4
	v_or_b32_e32 v5, 19, v2
	v_cmp_gt_i32_e64 s[24:25], v5, v4
	v_or_b32_e32 v5, 24, v2
	v_cmp_gt_i32_e64 s[26:27], v5, v4
	v_or_b32_e32 v5, 25, v2
	v_cmp_gt_i32_e32 vcc, v2, v4
	v_cmp_lt_i32_e64 s[4:5], v2, v4
	v_cmp_gt_i32_e64 s[28:29], v5, v4
	v_or_b32_e32 v5, 26, v2
	v_or_b32_e32 v2, 27, v2
	v_mad_u32_u24 v219, v193, s87, v6
	v_cmp_gt_i32_e64 s[30:31], v5, v4
	v_cmp_gt_i32_e64 s[34:35], v2, v4
	s_nop 1
	v_cndmask_b32_e64 v176, -1, 0, s[10:11]
	v_cndmask_b32_e64 v177, -1, 0, s[12:13]
	v_cndmask_b32_e64 v178, -1, 0, s[14:15]
	v_cndmask_b32_e64 v179, -1, 0, s[16:17]
	v_cndmask_b32_e64 v180, -1, 0, s[18:19]
	v_cndmask_b32_e64 v181, -1, 0, s[20:21]
	v_cndmask_b32_e64 v182, -1, 0, s[22:23]
	v_cndmask_b32_e64 v183, -1, 0, s[24:25]
	v_cndmask_b32_e64 v184, -1, 0, s[26:27]
	v_cndmask_b32_e64 v185, -1, 0, s[28:29]
	v_cndmask_b32_e64 v186, -1, 0, s[30:31]
	v_cndmask_b32_e64 v187, -1, 0, s[34:35]
	v_cndmask_b32_e64 v188, 0, -1, s[4:5]
	v_cndmask_b32_e64 v189, -1, 0, s[6:7]
	v_cndmask_b32_e64 v190, -1, 0, s[8:9]
	v_cndmask_b32_e64 v191, -1, 0, vcc
	v_or_b32_e32 v4, s63, v218
	v_add_u32_e32 v222, v219, v218
	v_lshl_add_u32 v4, v4, 1, v219
	ds_read_b128 v[84:87], v4 offset:17408
	ds_read_b128 v[88:91], v4 offset:8704
	v_add_u32_e32 v4, s64, v222
	v_add_u32_e32 v4, 0x2000, v4
	v_add_u32_e32 v220, s62, v226
	v_or_b32_e32 v2, s63, v193
	ds_read2_b64 v[92:95], v4 offset0:64 offset1:66
	v_or_b32_e32 v4, s65, v218
	v_mad_u32_u24 v2, v2, s86, v220
	v_lshl_add_u32 v4, v4, 1, v219
	ds_read_b128 v[96:99], v4 offset:17408
	ds_read_b128 v[194:197], v4 offset:8704
	ds_read_b128 v[198:201], v2 offset:26112
	ds_read_b128 v[202:205], v2 offset:26144
	v_add_u32_e32 v2, s66, v222
	v_add_u32_e32 v2, 0x2000, v2
	ds_read2_b64 v[206:209], v2 offset0:64 offset1:66
	v_or_b32_e32 v2, s67, v226
	v_add_u32_e32 v2, s62, v2
	ds_read_b128 v[4:7], v2 offset:41472
	ds_read_b128 v[8:11], v2 offset:41504
	ds_read_b128 v[12:15], v2 offset:44032
	ds_read_b128 v[16:19], v2 offset:44064
	ds_read_b128 v[20:23], v2 offset:41536
	ds_read_b128 v[24:27], v2 offset:41568
	ds_read_b128 v[28:31], v2 offset:44096
	ds_read_b128 v[32:35], v2 offset:44128
	s_waitcnt lgkmcnt(0)
	s_waitcnt lgkmcnt(1)
	v_pk_mul_f32 v[28:29], v[60:61], v[28:29]
	v_pk_mul_f32 v[30:31], v[62:63], v[30:31]
	s_waitcnt lgkmcnt(0)
; DI void h_chain(f32x16& S, f32x16& O, HPacks& K, const HOpsK& P, const bf16x8 (&vt)[2], const u32x4 (&vv)[2], int rq, int hh) {
;     f32x16 X;
;     { f32x16 Se;
; #pragma unroll
;       for (int g = 0; g < 4; ++g) {
; #pragma unroll
;           for (int e = 0; e < 4; ++e) Se[4 * g + e] = S[4 * g + e] * P.ebm[g][e]; }
;       K.sp0 = pack_step(Se, 0); K.sp1 = pack_step(Se, 1); }
; #pragma unroll
;     for (int g = 0; g < 4; ++g) {
; #pragma unroll
;         for (int e = 0; e < 4; ++e) S[4 * g + e] *= P.dec[g][e]; }
; #pragma unroll
;     for (int i = 0; i < 16; ++i) { X[i] = 0.f; O[i] = 0.f; }
;     __builtin_amdgcn_sched_barrier(0);
; #pragma unroll
;     for (int st = 0; st < 2; ++st) X = MFMA32(P.ka[st], P.qb[st], X);
; #pragma unroll
;     for (int i = 0; i < 16; ++i) X[i] = (crow(i, hh) <= rq) ? X[i] : 0.f;
;     K.xp0 = pack_step(X, 0); K.xp1 = pack_step(X, 1);
;     __builtin_amdgcn_sched_barrier(0);
;     O = MFMA32(K.xp0, __builtin_bit_cast(bf16x8, vv[0]), O);
;     O = MFMA32(__builtin_bit_cast(bf16x8, P.qq[0]), K.sp0, O);
;     O = MFMA32(K.xp1, __builtin_bit_cast(bf16x8, vv[1]), O);
;     O = MFMA32(__builtin_bit_cast(bf16x8, P.qq[1]), K.sp1, O);
; #pragma unroll
;     for (int st = 0; st < 2; ++st) S = MFMA32(P.ku[st], vt[st], S);
;     __builtin_amdgcn_sched_barrier(0);
; }
; DI void h_mma2(f32x16& S0, f32x16& S1, LAS unsigned char* buf, LAS unsigned char* red, int kbp, int vb, int r32, int hh) {
;     int rq = r32; asm volatile("" : "+v"(rq));
;     bf16x8 vt[2]; u32x4 vv[2];
; #pragma unroll
;     for (int st = 0; st < 2; ++st) {
;         vt[st] = *(const LAS bf16x8*)(buf + H_VT + (vb * 32 + r32) * 80 + (16 * st + 8 * hh) * 2);
;         const LAS unsigned char* vp = buf + H_VT + (vb * 32 + r32) * 80 + (16 * st + 4 * hh) * 2;
;         const u32x2 v0 = *(const LAS u32x2*)vp, v1 = *(const LAS u32x2*)(vp + 16);
;         vv[st].x = v0.x; vv[st].y = v0.y; vv[st].z = v1.x; vv[st].w = v1.y;
;     }
;     f32x16 Osum;
; #pragma unroll
;     for (int kk = 0; kk < 2; ++kk) {
;         HOpsK P; h_opsk_load(P, buf, 2 * kbp + kk, r32, hh);
;         f32x16& S = (kk == 0) ? S0 : S1; f32x16 O;
;         LDS_WAIT(); __builtin_amdgcn_sched_barrier(0);
;         HPacks K;
;         h_chain(S, O, K, P, vt, vv, rq, hh);
;         { float s_ = S[15] + O[15]; asm volatile("v_mov_b32 %0, %0" : "+v"(s_)); asm volatile("" :: "v"(s_)); }
	v_pk_mul_f32 v[32:33], v[64:65], v[32:33]
	v_pk_mul_f32 v[34:35], v[66:67], v[34:35]
	v_pk_mul_f32 v[12:13], v[52:53], v[12:13]
	v_pk_mul_f32 v[14:15], v[54:55], v[14:15]
	v_pk_mul_f32 v[16:17], v[56:57], v[16:17]
	v_pk_mul_f32 v[18:19], v[58:59], v[18:19]
	v_cvt_pk_bf16_f32 v214, v28, v29
	v_cvt_pk_bf16_f32 v215, v30, v31
	v_cvt_pk_bf16_f32 v216, v32, v33
	v_cvt_pk_bf16_f32 v217, v34, v35
	v_pk_mul_f32 v[34:35], v[66:67], v[26:27]
	v_pk_mul_f32 v[30:31], v[62:63], v[22:23]
	v_pk_mul_f32 v[26:27], v[58:59], v[10:11]
	v_pk_mul_f32 v[22:23], v[54:55], v[6:7]
	v_pk_mul_f32 v[32:33], v[64:65], v[24:25]
	v_pk_mul_f32 v[28:29], v[60:61], v[20:21]
	v_pk_mul_f32 v[24:25], v[56:57], v[8:9]
	v_pk_mul_f32 v[20:21], v[52:53], v[4:5]
	v_cvt_pk_bf16_f32 v210, v12, v13
	v_cvt_pk_bf16_f32 v211, v14, v15
	v_cvt_pk_bf16_f32 v212, v16, v17
	v_cvt_pk_bf16_f32 v213, v18, v19
	v_mfma_f32_32x32x16_bf16 v[4:19], v[84:87], v[88:91], 0
	v_mfma_f32_32x32x16_bf16 v[4:19], v[96:99], v[194:197], v[4:19]
	s_nop 11
	v_cndmask_b32_e64 v2, v4, 0, vcc
	v_cndmask_b32_e64 v4, 0, v5, s[4:5]
	v_cndmask_b32_e64 v5, v6, 0, s[6:7]
	v_cndmask_b32_e64 v6, v7, 0, s[8:9]
	v_cndmask_b32_e64 v7, v8, 0, s[10:11]
	v_cndmask_b32_e64 v8, v9, 0, s[12:13]
	v_cndmask_b32_e64 v9, v10, 0, s[14:15]
	v_cndmask_b32_e64 v10, v11, 0, s[16:17]
	v_cndmask_b32_e64 v11, v12, 0, s[18:19]
	v_cndmask_b32_e64 v12, v13, 0, s[20:21]
	v_cndmask_b32_e64 v13, v14, 0, s[22:23]
	v_cndmask_b32_e64 v14, v15, 0, s[24:25]
	v_cndmask_b32_e64 v15, v16, 0, s[26:27]
	v_cndmask_b32_e64 v16, v17, 0, s[28:29]
	v_cndmask_b32_e64 v17, v18, 0, s[30:31]
	v_cndmask_b32_e64 v18, v19, 0, s[34:35]
	v_cvt_pk_bf16_f32 v4, v2, v4
	v_cvt_pk_bf16_f32 v5, v5, v6
	v_cvt_pk_bf16_f32 v6, v7, v8
	v_cvt_pk_bf16_f32 v7, v9, v10
	v_cvt_pk_bf16_f32 v8, v11, v12
	v_cvt_pk_bf16_f32 v9, v13, v14
	v_cvt_pk_bf16_f32 v10, v15, v16
	v_cvt_pk_bf16_f32 v11, v17, v18
	v_mfma_f32_32x32x16_bf16 v[68:83], v[4:7], v[100:103], 0
	v_mfma_f32_32x32x16_bf16 v[68:83], v[92:95], v[210:213], v[68:83]
	v_mfma_f32_32x32x16_bf16 v[20:35], v[198:201], v[108:111], v[20:35]
	v_mfma_f32_32x32x16_bf16 v[68:83], v[8:11], v[104:107], v[68:83]
	v_mfma_f32_32x32x16_bf16 v[20:35], v[202:205], v[112:115], v[20:35]
	v_mfma_f32_32x32x16_bf16 v[68:83], v[206:209], v[214:217], v[68:83]
	s_nop 11
	v_add_f32_e32 v2, v83, v35
	v_mov_b32 v2, v2
	s_nop 0
	v_or_b32_e32 v4, s68, v218
	v_lshl_add_u32 v4, v4, 1, v219
	ds_read_b128 v[194:197], v4 offset:17408
	ds_read_b128 v[198:201], v4 offset:8704
	v_add_u32_e32 v4, s69, v222
	v_add_u32_e32 v4, 0x2000, v4
	v_or_b32_e32 v2, s68, v193
	ds_read2_b64 v[202:205], v4 offset0:64 offset1:66
	v_or_b32_e32 v4, s70, v218
	v_mad_u32_u24 v2, v2, s86, v220
	v_lshl_add_u32 v4, v4, 1, v219
	ds_read_b128 v[206:209], v4 offset:17408
	ds_read_b128 v[210:213], v4 offset:8704
	ds_read_b128 v[214:217], v2 offset:26112
	ds_read_b128 v[218:221], v2 offset:26144
	v_add_u32_e32 v2, s71, v222
	v_add_u32_e32 v2, 0x2000, v2
	ds_read2_b64 v[222:225], v2 offset0:64 offset1:66
	v_or_b32_e32 v2, s72, v226
	v_add_u32_e32 v2, s62, v2
	ds_read_b128 v[4:7], v2 offset:41472
	ds_read_b128 v[8:11], v2 offset:41504
	ds_read_b128 v[12:15], v2 offset:44032
	ds_read_b128 v[16:19], v2 offset:44064
	ds_read_b128 v[84:87], v2 offset:41536
	ds_read_b128 v[88:91], v2 offset:41568
	ds_read_b128 v[92:95], v2 offset:44096
	ds_read_b128 v[96:99], v2 offset:44128
	s_waitcnt lgkmcnt(0)
	s_waitcnt lgkmcnt(5)
	v_pk_mul_f32 v[12:13], v[36:37], v[12:13]
	v_pk_mul_f32 v[14:15], v[38:39], v[14:15]
	s_waitcnt lgkmcnt(4)
	v_pk_mul_f32 v[16:17], v[40:41], v[16:17]
	v_pk_mul_f32 v[18:19], v[42:43], v[18:19]
	s_waitcnt lgkmcnt(1)
	v_pk_mul_f32 v[92:93], v[44:45], v[92:93]
	v_pk_mul_f32 v[94:95], v[46:47], v[94:95]
	s_waitcnt lgkmcnt(0)
	v_pk_mul_f32 v[96:97], v[48:49], v[96:97]
	v_pk_mul_f32 v[98:99], v[50:51], v[98:99]
	v_cvt_pk_bf16_f32 v226, v12, v13
	v_cvt_pk_bf16_f32 v227, v14, v15
	v_cvt_pk_bf16_f32 v228, v16, v17
	v_cvt_pk_bf16_f32 v229, v18, v19
	v_pk_mul_f32 v[18:19], v[50:51], v[90:91]
	v_pk_mul_f32 v[14:15], v[46:47], v[86:87]
	v_pk_mul_f32 v[10:11], v[42:43], v[10:11]
	v_pk_mul_f32 v[6:7], v[38:39], v[6:7]
	v_pk_mul_f32 v[16:17], v[48:49], v[88:89]
	v_pk_mul_f32 v[12:13], v[44:45], v[84:85]
	v_pk_mul_f32 v[8:9], v[40:41], v[8:9]
	v_pk_mul_f32 v[4:5], v[36:37], v[4:5]
	v_cvt_pk_bf16_f32 v230, v92, v93
	v_cvt_pk_bf16_f32 v231, v94, v95
	v_cvt_pk_bf16_f32 v232, v96, v97
	v_cvt_pk_bf16_f32 v233, v98, v99
	v_mfma_f32_32x32x16_bf16 v[84:99], v[194:197], v[198:201], 0
	v_mfma_f32_32x32x16_bf16 v[84:99], v[206:209], v[210:213], v[84:99]
	s_nop 11
	v_cndmask_b32_e64 v2, v84, 0, vcc
	v_cndmask_b32_e64 v84, 0, v85, s[4:5]
	v_cndmask_b32_e64 v85, v86, 0, s[6:7]
	v_cndmask_b32_e64 v86, v87, 0, s[8:9]
	v_cndmask_b32_e64 v87, v88, 0, s[10:11]
	v_cndmask_b32_e64 v88, v89, 0, s[12:13]
	v_cndmask_b32_e64 v89, v90, 0, s[14:15]
	v_cndmask_b32_e64 v90, v91, 0, s[16:17]
	v_cndmask_b32_e64 v91, v92, 0, s[18:19]
	v_cndmask_b32_e64 v92, v93, 0, s[20:21]
	v_cndmask_b32_e64 v93, v94, 0, s[22:23]
	v_cndmask_b32_e64 v94, v95, 0, s[24:25]
	v_cndmask_b32_e64 v95, v96, 0, s[26:27]
	v_cndmask_b32_e64 v96, v97, 0, s[28:29]
	v_cndmask_b32_e64 v97, v98, 0, s[30:31]
	v_cndmask_b32_e64 v98, v99, 0, s[34:35]
	v_cvt_pk_bf16_f32 v234, v2, v84
	v_cvt_pk_bf16_f32 v235, v85, v86
	v_cvt_pk_bf16_f32 v236, v87, v88
	v_cvt_pk_bf16_f32 v237, v89, v90
	v_cvt_pk_bf16_f32 v238, v91, v92
	v_cvt_pk_bf16_f32 v239, v93, v94
	v_cvt_pk_bf16_f32 v240, v95, v96
	v_cvt_pk_bf16_f32 v241, v97, v98
	v_mfma_f32_32x32x16_bf16 v[84:99], v[234:237], v[100:103], 0
	v_mfma_f32_32x32x16_bf16 v[84:99], v[202:205], v[226:229], v[84:99]
	v_mfma_f32_32x32x16_bf16 v[4:19], v[214:217], v[108:111], v[4:19]
	v_mfma_f32_32x32x16_bf16 v[84:99], v[238:241], v[104:107], v[84:99]
	v_mfma_f32_32x32x16_bf16 v[4:19], v[218:221], v[112:115], v[4:19]
	v_mfma_f32_32x32x16_bf16 v[84:99], v[222:225], v[230:233], v[84:99]
	s_nop 11
	v_add_f32_e32 v2, v99, v19
	v_mov_b32 v2, v2
	s_nop 0
	v_add_f32_e32 v2, v83, v99
	v_add_f32_e32 v82, v82, v98
	v_add_f32_e32 v81, v81, v97
	v_add_f32_e32 v80, v80, v96
	v_add_f32_e32 v79, v79, v95
	v_add_f32_e32 v78, v78, v94
	v_add_f32_e32 v77, v77, v93
	v_add_f32_e32 v76, v76, v92
	v_add_f32_e32 v75, v75, v91
	v_add_f32_e32 v74, v74, v90
	v_add_f32_e32 v73, v73, v89
	v_add_f32_e32 v72, v72, v88
	v_add_f32_e32 v71, v71, v87
	v_add_f32_e32 v70, v70, v86
	v_add_f32_e32 v69, v69, v85
	v_add_f32_e32 v68, v68, v84
	v_add_u32_e32 v83, 0x16800, v242
	ds_write2st64_b32 v83, v68, v69 offset1:1
	ds_write2st64_b32 v83, v70, v71 offset0:2 offset1:3
	ds_write2st64_b32 v83, v72, v73 offset0:8 offset1:9
	ds_write2st64_b32 v83, v74, v75 offset0:10 offset1:11
	ds_write2st64_b32 v83, v76, v77 offset0:16 offset1:17
	ds_write2st64_b32 v83, v78, v79 offset0:18 offset1:19
	ds_write2st64_b32 v83, v80, v81 offset0:24 offset1:25
	ds_write2st64_b32 v83, v82, v2 offset0:26 offset1:27
	s_mov_b64 s[4:5], 0

; #define LAS __attribute__((address_space(3)))
; #define LDS_WAIT() asm volatile("s_waitcnt lgkmcnt(0)" ::: "memory")
; DI int crow(int reg, int h) { return (reg & 3) + 8 * (reg >> 2) + 4 * h; }
; DI void h_mma2(f32x16& S0, f32x16& S1, LAS unsigned char* buf, LAS unsigned char* red, int kbp, int vb, int r32, int hh) {
;     int rq = r32; asm volatile("" : "+v"(rq));
;     bf16x8 vt[2]; u32x4 vv[2];
; #pragma unroll
;     for (int st = 0; st < 2; ++st) {
;         vt[st] = *(const LAS bf16x8*)(buf + H_VT + (vb * 32 + r32) * 80 + (16 * st + 8 * hh) * 2);
;         const LAS unsigned char* vp = buf + H_VT + (vb * 32 + r32) * 80 + (16 * st + 4 * hh) * 2;
;         const u32x2 v0 = *(const LAS u32x2*)vp, v1 = *(const LAS u32x2*)(vp + 16);
;         vv[st].x = v0.x; vv[st].y = v0.y; vv[st].z = v1.x; vv[st].w = v1.y;
;     }
;     f32x16 Osum;
; #pragma unroll
;     for (int kk = 0; kk < 2; ++kk) {
;         HOpsK P; h_opsk_load(P, buf, 2 * kbp + kk, r32, hh);
;         f32x16& S = (kk == 0) ? S0 : S1; f32x16 O;
;         LDS_WAIT(); __builtin_amdgcn_sched_barrier(0);
;         HPacks K;
;         h_chain(S, O, K, P, vt, vv, rq, hh);
;         { float s_ = S[15] + O[15]; asm volatile("v_mov_b32 %0, %0" : "+v"(s_)); asm volatile("" :: "v"(s_)); }
;         asm volatile("" :: "v"(P.ka[0]), "v"(P.ka[1]), "v"(P.qb[0]), "v"(P.qb[1]), "v"(P.ku[0]), "v"(P.ku[1]), "v"(P.qq[0]), "v"(P.qq[1]));
;         asm volatile("" :: "v"(K.sp0), "v"(K.sp1), "v"(K.xp0), "v"(K.xp1));
;         __builtin_amdgcn_sched_barrier(0);
; #pragma unroll
;         for (int i = 0; i < 16; ++i) Osum[i] = (kk == 0) ? O[i] : Osum[i] + O[i];
;         __builtin_amdgcn_sched_barrier(0);
;     }
;     asm volatile("" :: "v"(vt[0]), "v"(vt[1]), "v"(vv[0]), "v"(vv[1]));
; #pragma unroll
;     for (int i = 0; i < 16; ++i) *(LAS float*)(red + ((kbp * 32 + crow(i, hh)) * 64 + vb * 32 + r32) * 4) = Osum[i];
.LBB0_420:
	s_mov_b64 s[4:5], -1
	s_and_b64 vcc, exec, s[42:43]
	s_waitcnt lgkmcnt(0)
	s_barrier
	s_cbranch_vccz .LBB0_422
	s_andn2_b32 s4, 1, s39
	v_mov_b32_e32 v2, v0
	s_mul_i32 s5, s4, 0xb400
	s_add_i32 s62, s5, 0
	v_and_b32_e32 v193, 31, v2
	v_bfe_u32 v2, v2, 5, 1
	v_or_b32_e32 v37, s3, v193
	v_mov_b32_e32 v38, s62
	s_lshl_b32 s4, s4, 14
	v_lshlrev_b32_e32 v36, 8, v2
	v_mad_u32_u24 v37, v37, s86, v38
	v_lshlrev_b32_e32 v226, 4, v2
	v_lshlrev_b32_e32 v210, 3, v2
	s_add_i32 s4, s4, 0
	v_or3_b32 v36, v36, s73, v193
	v_add_u32_e32 v39, v37, v226
	v_add_u32_e32 v37, v37, v210
	v_lshl_add_u32 v242, v36, 2, s4
	v_mov_b32_e32 v36, v193
	v_add_u32_e32 v37, 0x8800, v37
	v_lshlrev_b32_e32 v2, 2, v2
	ds_read2_b64 v[100:103], v37 offset0:192 offset1:194
	ds_read2_b64 v[104:107], v37 offset0:196 offset1:198
	ds_read_b128 v[108:111], v39 offset:36352
	ds_read_b128 v[112:115], v39 offset:36384
	v_mad_u32_u24 v211, v193, s87, v38
	v_or_b32_e32 v36, s63, v210
	v_add_u32_e32 v222, v211, v210
	v_lshl_add_u32 v36, v36, 1, v211
	ds_read_b128 v[68:71], v36 offset:17408
	ds_read_b128 v[72:75], v36 offset:8704
	v_add_u32_e32 v36, s64, v222
	v_add_u32_e32 v36, 0x2000, v36
	v_add_u32_e32 v212, s62, v226
	v_or_b32_e32 v2, s63, v193
	ds_read2_b64 v[76:79], v36 offset0:64 offset1:66
	v_or_b32_e32 v36, s65, v210
	v_mad_u32_u24 v2, v2, s86, v212
	v_lshl_add_u32 v36, v36, 1, v211
	ds_read_b128 v[80:83], v36 offset:17408
	ds_read_b128 v[84:87], v36 offset:8704
	ds_read_b128 v[88:91], v2 offset:26112
	ds_read_b128 v[92:95], v2 offset:26144
	v_add_u32_e32 v2, s66, v222
	v_add_u32_e32 v2, 0x2000, v2
	ds_read2_b64 v[96:99], v2 offset0:64 offset1:66
	v_or_b32_e32 v2, s67, v226
	v_add_u32_e32 v2, s62, v2
	ds_read_b128 v[36:39], v2 offset:41472
	ds_read_b128 v[40:43], v2 offset:41504
	ds_read_b128 v[44:47], v2 offset:44032
	ds_read_b128 v[48:51], v2 offset:44064
	ds_read_b128 v[52:55], v2 offset:41536
	ds_read_b128 v[56:59], v2 offset:41568
	ds_read_b128 v[60:63], v2 offset:44096
	ds_read_b128 v[64:67], v2 offset:44128
	s_waitcnt lgkmcnt(0)
	s_waitcnt lgkmcnt(5)
	v_pk_mul_f32 v[44:45], v[20:21], v[44:45]
	v_pk_mul_f32 v[46:47], v[22:23], v[46:47]
	s_waitcnt lgkmcnt(4)
	v_pk_mul_f32 v[48:49], v[24:25], v[48:49]
	v_pk_mul_f32 v[50:51], v[26:27], v[50:51]
	s_waitcnt lgkmcnt(1)
	v_pk_mul_f32 v[60:61], v[28:29], v[60:61]
	v_pk_mul_f32 v[62:63], v[30:31], v[62:63]
	s_waitcnt lgkmcnt(0)
	v_pk_mul_f32 v[64:65], v[32:33], v[64:65]
	v_pk_mul_f32 v[66:67], v[34:35], v[66:67]
	v_cvt_pk_bf16_f32 v194, v44, v45
	v_cvt_pk_bf16_f32 v195, v46, v47
	v_cvt_pk_bf16_f32 v196, v48, v49
	v_cvt_pk_bf16_f32 v197, v50, v51
	v_pk_mul_f32 v[50:51], v[34:35], v[58:59]
	v_pk_mul_f32 v[46:47], v[30:31], v[54:55]
	v_pk_mul_f32 v[42:43], v[26:27], v[42:43]
	v_pk_mul_f32 v[38:39], v[22:23], v[38:39]
	v_pk_mul_f32 v[48:49], v[32:33], v[56:57]
	v_pk_mul_f32 v[44:45], v[28:29], v[52:53]
	v_pk_mul_f32 v[40:41], v[24:25], v[40:41]
	v_pk_mul_f32 v[36:37], v[20:21], v[36:37]
	v_cvt_pk_bf16_f32 v198, v60, v61
	v_cvt_pk_bf16_f32 v199, v62, v63
	v_cvt_pk_bf16_f32 v200, v64, v65
	v_cvt_pk_bf16_f32 v201, v66, v67
	v_mfma_f32_32x32x16_bf16 v[52:67], v[68:71], v[72:75], 0
	v_mfma_f32_32x32x16_bf16 v[52:67], v[80:83], v[84:87], v[52:67]
	s_nop 11
	v_and_b32_e32 v2, v191, v52
	v_and_b32_e32 v52, v188, v53
	v_and_b32_e32 v53, v189, v54
	v_and_b32_e32 v54, v190, v55
	v_and_b32_e32 v55, v176, v56
	v_and_b32_e32 v56, v177, v57
	v_and_b32_e32 v57, v178, v58
	v_and_b32_e32 v58, v179, v59
	v_and_b32_e32 v59, v180, v60
	v_and_b32_e32 v60, v181, v61
	v_and_b32_e32 v61, v182, v62
	v_and_b32_e32 v62, v183, v63
	v_and_b32_e32 v63, v184, v64
	v_and_b32_e32 v64, v185, v65
	v_and_b32_e32 v65, v186, v66
	v_and_b32_e32 v66, v187, v67
	v_cvt_pk_bf16_f32 v202, v2, v52
	v_cvt_pk_bf16_f32 v203, v53, v54
	v_cvt_pk_bf16_f32 v204, v55, v56
	v_cvt_pk_bf16_f32 v205, v57, v58
	v_cvt_pk_bf16_f32 v206, v59, v60
	v_cvt_pk_bf16_f32 v207, v61, v62
	v_cvt_pk_bf16_f32 v208, v63, v64
	v_cvt_pk_bf16_f32 v209, v65, v66
	v_mfma_f32_32x32x16_bf16 v[52:67], v[202:205], v[100:103], 0
	v_mfma_f32_32x32x16_bf16 v[52:67], v[76:79], v[194:197], v[52:67]
	v_mfma_f32_32x32x16_bf16 v[36:51], v[88:91], v[108:111], v[36:51]
	v_mfma_f32_32x32x16_bf16 v[52:67], v[206:209], v[104:107], v[52:67]
	v_mfma_f32_32x32x16_bf16 v[36:51], v[92:95], v[112:115], v[36:51]
	v_mfma_f32_32x32x16_bf16 v[52:67], v[96:99], v[198:201], v[52:67]
	s_nop 11
	v_add_f32_e32 v2, v67, v51
	v_mov_b32 v2, v2
	s_nop 0
	v_or_b32_e32 v68, s68, v210
	v_lshl_add_u32 v68, v68, 1, v211
	ds_read_b128 v[194:197], v68 offset:17408
	ds_read_b128 v[198:201], v68 offset:8704
	v_add_u32_e32 v68, s69, v222
	v_add_u32_e32 v68, 0x2000, v68
	v_or_b32_e32 v2, s68, v193
	ds_read2_b64 v[202:205], v68 offset0:64 offset1:66
	v_or_b32_e32 v68, s70, v210
	v_mad_u32_u24 v2, v2, s86, v212
	v_lshl_add_u32 v68, v68, 1, v211
	ds_read_b128 v[206:209], v68 offset:17408
	ds_read_b128 v[210:213], v68 offset:8704
	ds_read_b128 v[214:217], v2 offset:26112
	ds_read_b128 v[218:221], v2 offset:26144
	v_add_u32_e32 v2, s71, v222
	v_add_u32_e32 v2, 0x2000, v2
	ds_read2_b64 v[222:225], v2 offset0:64 offset1:66
	v_or_b32_e32 v2, s72, v226
	v_add_u32_e32 v2, s62, v2
	ds_read_b128 v[68:71], v2 offset:41472
	ds_read_b128 v[72:75], v2 offset:41504
	ds_read_b128 v[76:79], v2 offset:44032
	ds_read_b128 v[80:83], v2 offset:44064
	ds_read_b128 v[84:87], v2 offset:41536
	ds_read_b128 v[88:91], v2 offset:41568
	ds_read_b128 v[92:95], v2 offset:44096
	ds_read_b128 v[96:99], v2 offset:44128
	s_waitcnt lgkmcnt(0)
; DI void h_chain(f32x16& S, f32x16& O, HPacks& K, const HOpsK& P, const bf16x8 (&vt)[2], const u32x4 (&vv)[2], int rq, int hh) {
;     f32x16 X;
;     { f32x16 Se;
; #pragma unroll
;       for (int g = 0; g < 4; ++g) {
; #pragma unroll
;           for (int e = 0; e < 4; ++e) Se[4 * g + e] = S[4 * g + e] * P.ebm[g][e]; }
;       K.sp0 = pack_step(Se, 0); K.sp1 = pack_step(Se, 1); }
; #pragma unroll
;     for (int g = 0; g < 4; ++g) {
; #pragma unroll
;         for (int e = 0; e < 4; ++e) S[4 * g + e] *= P.dec[g][e]; }
; #pragma unroll
;     for (int i = 0; i < 16; ++i) { X[i] = 0.f; O[i] = 0.f; }
;     __builtin_amdgcn_sched_barrier(0);
; #pragma unroll
;     for (int st = 0; st < 2; ++st) X = MFMA32(P.ka[st], P.qb[st], X);
; #pragma unroll
;     for (int i = 0; i < 16; ++i) X[i] = (crow(i, hh) <= rq) ? X[i] : 0.f;
;     K.xp0 = pack_step(X, 0); K.xp1 = pack_step(X, 1);
;     __builtin_amdgcn_sched_barrier(0);
;     O = MFMA32(K.xp0, __builtin_bit_cast(bf16x8, vv[0]), O);
;     O = MFMA32(__builtin_bit_cast(bf16x8, P.qq[0]), K.sp0, O);
;     O = MFMA32(K.xp1, __builtin_bit_cast(bf16x8, vv[1]), O);
;     O = MFMA32(__builtin_bit_cast(bf16x8, P.qq[1]), K.sp1, O);
; #pragma unroll
;     for (int st = 0; st < 2; ++st) S = MFMA32(P.ku[st], vt[st], S);
;     __builtin_amdgcn_sched_barrier(0);
; }
; DI void h_mma2(f32x16& S0, f32x16& S1, LAS unsigned char* buf, LAS unsigned char* red, int kbp, int vb, int r32, int hh) {
;     int rq = r32; asm volatile("" : "+v"(rq));
;     bf16x8 vt[2]; u32x4 vv[2];
; #pragma unroll
;     for (int st = 0; st < 2; ++st) {
;         vt[st] = *(const LAS bf16x8*)(buf + H_VT + (vb * 32 + r32) * 80 + (16 * st + 8 * hh) * 2);
;         const LAS unsigned char* vp = buf + H_VT + (vb * 32 + r32) * 80 + (16 * st + 4 * hh) * 2;
;         const u32x2 v0 = *(const LAS u32x2*)vp, v1 = *(const LAS u32x2*)(vp + 16);
;         vv[st].x = v0.x; vv[st].y = v0.y; vv[st].z = v1.x; vv[st].w = v1.y;
;     }
;     f32x16 Osum;
; #pragma unroll
;     for (int kk = 0; kk < 2; ++kk) {
;         HOpsK P; h_opsk_load(P, buf, 2 * kbp + kk, r32, hh);
;         f32x16& S = (kk == 0) ? S0 : S1; f32x16 O;
;         LDS_WAIT(); __builtin_amdgcn_sched_barrier(0);
;         HPacks K;
;         h_chain(S, O, K, P, vt, vv, rq, hh);
;         { float s_ = S[15] + O[15]; asm volatile("v_mov_b32 %0, %0" : "+v"(s_)); asm volatile("" :: "v"(s_)); }
	s_waitcnt lgkmcnt(5)
	v_pk_mul_f32 v[76:77], v[4:5], v[76:77]
	v_pk_mul_f32 v[78:79], v[6:7], v[78:79]
	s_waitcnt lgkmcnt(4)
	v_pk_mul_f32 v[80:81], v[8:9], v[80:81]
	v_pk_mul_f32 v[82:83], v[10:11], v[82:83]
	s_waitcnt lgkmcnt(1)
	v_pk_mul_f32 v[92:93], v[12:13], v[92:93]
	v_pk_mul_f32 v[94:95], v[14:15], v[94:95]
	s_waitcnt lgkmcnt(0)
	v_pk_mul_f32 v[96:97], v[16:17], v[96:97]
	v_pk_mul_f32 v[98:99], v[18:19], v[98:99]
	v_cvt_pk_bf16_f32 v226, v76, v77
	v_cvt_pk_bf16_f32 v227, v78, v79
	v_cvt_pk_bf16_f32 v228, v80, v81
	v_cvt_pk_bf16_f32 v229, v82, v83
	v_pk_mul_f32 v[82:83], v[18:19], v[90:91]
	v_pk_mul_f32 v[78:79], v[14:15], v[86:87]
	v_pk_mul_f32 v[74:75], v[10:11], v[74:75]
	v_pk_mul_f32 v[70:71], v[6:7], v[70:71]
	v_pk_mul_f32 v[80:81], v[16:17], v[88:89]
	v_pk_mul_f32 v[76:77], v[12:13], v[84:85]
	v_pk_mul_f32 v[72:73], v[8:9], v[72:73]
	v_pk_mul_f32 v[68:69], v[4:5], v[68:69]
	v_cvt_pk_bf16_f32 v230, v92, v93
	v_cvt_pk_bf16_f32 v231, v94, v95
	v_cvt_pk_bf16_f32 v232, v96, v97
	v_cvt_pk_bf16_f32 v233, v98, v99
	v_mfma_f32_32x32x16_bf16 v[84:99], v[194:197], v[198:201], 0
	v_mfma_f32_32x32x16_bf16 v[84:99], v[206:209], v[210:213], v[84:99]
	s_nop 11
	v_and_b32_e32 v2, v191, v84
	v_and_b32_e32 v84, v188, v85
	v_and_b32_e32 v85, v189, v86
	v_and_b32_e32 v86, v190, v87
	v_and_b32_e32 v87, v176, v88
	v_and_b32_e32 v88, v177, v89
	v_and_b32_e32 v89, v178, v90
	v_and_b32_e32 v90, v179, v91
	v_and_b32_e32 v91, v180, v92
	v_and_b32_e32 v92, v181, v93
	v_and_b32_e32 v93, v182, v94
	v_and_b32_e32 v94, v183, v95
	v_and_b32_e32 v95, v184, v96
	v_and_b32_e32 v96, v185, v97
	v_and_b32_e32 v97, v186, v98
	v_and_b32_e32 v98, v187, v99
	v_cvt_pk_bf16_f32 v234, v2, v84
	v_cvt_pk_bf16_f32 v235, v85, v86
	v_cvt_pk_bf16_f32 v236, v87, v88
	v_cvt_pk_bf16_f32 v237, v89, v90
	v_cvt_pk_bf16_f32 v238, v91, v92
	v_cvt_pk_bf16_f32 v239, v93, v94
	v_cvt_pk_bf16_f32 v240, v95, v96
	v_cvt_pk_bf16_f32 v241, v97, v98
	v_mfma_f32_32x32x16_bf16 v[84:99], v[234:237], v[100:103], 0
	v_mfma_f32_32x32x16_bf16 v[84:99], v[202:205], v[226:229], v[84:99]
	v_mfma_f32_32x32x16_bf16 v[68:83], v[214:217], v[108:111], v[68:83]
	v_mfma_f32_32x32x16_bf16 v[84:99], v[238:241], v[104:107], v[84:99]
	v_mfma_f32_32x32x16_bf16 v[68:83], v[218:221], v[112:115], v[68:83]
	v_mfma_f32_32x32x16_bf16 v[84:99], v[222:225], v[230:233], v[84:99]
	s_nop 11
	v_add_f32_e32 v2, v99, v83
	v_mov_b32 v2, v2
	s_nop 0
	v_add_f32_e32 v2, v67, v99
	v_add_f32_e32 v66, v66, v98
	v_add_f32_e32 v65, v65, v97
	v_add_f32_e32 v64, v64, v96
	v_add_f32_e32 v63, v63, v95
	v_add_f32_e32 v62, v62, v94
	v_add_f32_e32 v61, v61, v93
	v_add_f32_e32 v60, v60, v92
	v_add_f32_e32 v59, v59, v91
	v_add_f32_e32 v58, v58, v90
	v_add_f32_e32 v57, v57, v89
	v_add_f32_e32 v56, v56, v88
	v_add_f32_e32 v55, v55, v87
	v_add_f32_e32 v54, v54, v86
	v_add_f32_e32 v53, v53, v85
	v_add_f32_e32 v52, v52, v84
	v_add_u32_e32 v67, 0x16800, v242
	ds_write2st64_b32 v67, v52, v53 offset1:1
	ds_write2st64_b32 v67, v54, v55 offset0:2 offset1:3
	ds_write2st64_b32 v67, v56, v57 offset0:8 offset1:9
	ds_write2st64_b32 v67, v58, v59 offset0:10 offset1:11
	ds_write2st64_b32 v67, v60, v61 offset0:16 offset1:17
	ds_write2st64_b32 v67, v62, v63 offset0:18 offset1:19
	ds_write2st64_b32 v67, v64, v65 offset0:24 offset1:25
	ds_write2st64_b32 v67, v66, v2 offset0:26 offset1:27
	s_mov_b64 s[4:5], 0

; #define LAS __attribute__((address_space(3)))
; #define LDS_WAIT() asm volatile("s_waitcnt lgkmcnt(0)" ::: "memory")
; DI int crow(int reg, int h) { return (reg & 3) + 8 * (reg >> 2) + 4 * h; }
; DI void h_mma2(f32x16& S0, f32x16& S1, LAS unsigned char* buf, LAS unsigned char* red, int kbp, int vb, int r32, int hh) {
;     int rq = r32; asm volatile("" : "+v"(rq));
;     bf16x8 vt[2]; u32x4 vv[2];
; #pragma unroll
;     for (int st = 0; st < 2; ++st) {
;         vt[st] = *(const LAS bf16x8*)(buf + H_VT + (vb * 32 + r32) * 80 + (16 * st + 8 * hh) * 2);
;         const LAS unsigned char* vp = buf + H_VT + (vb * 32 + r32) * 80 + (16 * st + 4 * hh) * 2;
;         const u32x2 v0 = *(const LAS u32x2*)vp, v1 = *(const LAS u32x2*)(vp + 16);
;         vv[st].x = v0.x; vv[st].y = v0.y; vv[st].z = v1.x; vv[st].w = v1.y;
;     }
;     f32x16 Osum;
; #pragma unroll
;     for (int kk = 0; kk < 2; ++kk) {
;         HOpsK P; h_opsk_load(P, buf, 2 * kbp + kk, r32, hh);
;         f32x16& S = (kk == 0) ? S0 : S1; f32x16 O;
;         LDS_WAIT(); __builtin_amdgcn_sched_barrier(0);
;         HPacks K;
;         h_chain(S, O, K, P, vt, vv, rq, hh);
;         { float s_ = S[15] + O[15]; asm volatile("v_mov_b32 %0, %0" : "+v"(s_)); asm volatile("" :: "v"(s_)); }
;         asm volatile("" :: "v"(P.ka[0]), "v"(P.ka[1]), "v"(P.qb[0]), "v"(P.qb[1]), "v"(P.ku[0]), "v"(P.ku[1]), "v"(P.qq[0]), "v"(P.qq[1]));
;         asm volatile("" :: "v"(K.sp0), "v"(K.sp1), "v"(K.xp0), "v"(K.xp1));
;         __builtin_amdgcn_sched_barrier(0);
; #pragma unroll
;         for (int i = 0; i < 16; ++i) Osum[i] = (kk == 0) ? O[i] : Osum[i] + O[i];
;         __builtin_amdgcn_sched_barrier(0);
;     }
;     asm volatile("" :: "v"(vt[0]), "v"(vt[1]), "v"(vv[0]), "v"(vv[1]));
; #pragma unroll
;     for (int i = 0; i < 16; ++i) *(LAS float*)(red + ((kbp * 32 + crow(i, hh)) * 64 + vb * 32 + r32) * 4) = Osum[i];
.LBB0_429:
	s_mov_b64 s[4:5], -1
	s_and_b64 vcc, exec, s[42:43]
	s_waitcnt lgkmcnt(0)
	s_barrier
	s_cbranch_vccz .LBB0_431
	s_and_b32 s4, s39, 1
	v_mov_b32_e32 v2, v0
	s_mul_i32 s5, s4, 0xb400
	s_add_i32 s62, s5, 0
	v_and_b32_e32 v193, 31, v2
	v_bfe_u32 v2, v2, 5, 1
	v_or_b32_e32 v37, s3, v193
	v_mov_b32_e32 v38, s62
	s_lshl_b32 s4, s4, 14
	v_lshlrev_b32_e32 v36, 8, v2
	v_mad_u32_u24 v37, v37, s86, v38
	v_lshlrev_b32_e32 v226, 4, v2
	v_lshlrev_b32_e32 v210, 3, v2
	s_add_i32 s4, s4, 0
	v_or3_b32 v36, v36, s73, v193
	v_add_u32_e32 v39, v37, v226
	v_add_u32_e32 v37, v37, v210
	v_lshl_add_u32 v242, v36, 2, s4
	v_mov_b32_e32 v36, v193
	v_add_u32_e32 v37, 0x8800, v37
	v_lshlrev_b32_e32 v2, 2, v2
	ds_read2_b64 v[100:103], v37 offset0:192 offset1:194
	ds_read2_b64 v[104:107], v37 offset0:196 offset1:198
	ds_read_b128 v[108:111], v39 offset:36352
	ds_read_b128 v[112:115], v39 offset:36384
	v_mad_u32_u24 v211, v193, s87, v38
	v_or_b32_e32 v36, s63, v210
	v_add_u32_e32 v222, v211, v210
	v_lshl_add_u32 v36, v36, 1, v211
	ds_read_b128 v[68:71], v36 offset:17408
	ds_read_b128 v[72:75], v36 offset:8704
	v_add_u32_e32 v36, s64, v222
	v_add_u32_e32 v36, 0x2000, v36
	v_add_u32_e32 v212, s62, v226
	v_or_b32_e32 v2, s63, v193
	ds_read2_b64 v[76:79], v36 offset0:64 offset1:66
	v_or_b32_e32 v36, s65, v210
	v_mad_u32_u24 v2, v2, s86, v212
	v_lshl_add_u32 v36, v36, 1, v211
	ds_read_b128 v[80:83], v36 offset:17408
	ds_read_b128 v[84:87], v36 offset:8704
	ds_read_b128 v[88:91], v2 offset:26112
	ds_read_b128 v[92:95], v2 offset:26144
	v_add_u32_e32 v2, s66, v222
	v_add_u32_e32 v2, 0x2000, v2
	ds_read2_b64 v[96:99], v2 offset0:64 offset1:66
	v_or_b32_e32 v2, s67, v226
	v_add_u32_e32 v2, s62, v2
	ds_read_b128 v[36:39], v2 offset:41472
	ds_read_b128 v[40:43], v2 offset:41504
	ds_read_b128 v[44:47], v2 offset:44032
	ds_read_b128 v[48:51], v2 offset:44064
	ds_read_b128 v[52:55], v2 offset:41536
	ds_read_b128 v[56:59], v2 offset:41568
	ds_read_b128 v[60:63], v2 offset:44096
	ds_read_b128 v[64:67], v2 offset:44128
	s_waitcnt lgkmcnt(0)
	s_waitcnt lgkmcnt(5)
	v_pk_mul_f32 v[44:45], v[20:21], v[44:45]
	v_pk_mul_f32 v[46:47], v[22:23], v[46:47]
	s_waitcnt lgkmcnt(4)
	v_pk_mul_f32 v[48:49], v[24:25], v[48:49]
	v_pk_mul_f32 v[50:51], v[26:27], v[50:51]
	s_waitcnt lgkmcnt(1)
	v_pk_mul_f32 v[60:61], v[28:29], v[60:61]
	v_pk_mul_f32 v[62:63], v[30:31], v[62:63]
	s_waitcnt lgkmcnt(0)
	v_pk_mul_f32 v[64:65], v[32:33], v[64:65]
	v_pk_mul_f32 v[66:67], v[34:35], v[66:67]
	v_cvt_pk_bf16_f32 v194, v44, v45
	v_cvt_pk_bf16_f32 v195, v46, v47
	v_cvt_pk_bf16_f32 v196, v48, v49
	v_cvt_pk_bf16_f32 v197, v50, v51
	v_pk_mul_f32 v[50:51], v[34:35], v[58:59]
	v_pk_mul_f32 v[46:47], v[30:31], v[54:55]
	v_pk_mul_f32 v[42:43], v[26:27], v[42:43]
	v_pk_mul_f32 v[38:39], v[22:23], v[38:39]
	v_pk_mul_f32 v[48:49], v[32:33], v[56:57]
	v_pk_mul_f32 v[44:45], v[28:29], v[52:53]
	v_pk_mul_f32 v[40:41], v[24:25], v[40:41]
	v_pk_mul_f32 v[36:37], v[20:21], v[36:37]
	v_cvt_pk_bf16_f32 v198, v60, v61
	v_cvt_pk_bf16_f32 v199, v62, v63
	v_cvt_pk_bf16_f32 v200, v64, v65
	v_cvt_pk_bf16_f32 v201, v66, v67
	v_mfma_f32_32x32x16_bf16 v[52:67], v[68:71], v[72:75], 0
	v_mfma_f32_32x32x16_bf16 v[52:67], v[80:83], v[84:87], v[52:67]
	s_nop 11
	v_and_b32_e32 v2, v191, v52
	v_and_b32_e32 v52, v188, v53
	v_and_b32_e32 v53, v189, v54
	v_and_b32_e32 v54, v190, v55
	v_and_b32_e32 v55, v176, v56
	v_and_b32_e32 v56, v177, v57
	v_and_b32_e32 v57, v178, v58
	v_and_b32_e32 v58, v179, v59
	v_and_b32_e32 v59, v180, v60
	v_and_b32_e32 v60, v181, v61
	v_and_b32_e32 v61, v182, v62
	v_and_b32_e32 v62, v183, v63
	v_and_b32_e32 v63, v184, v64
	v_and_b32_e32 v64, v185, v65
	v_and_b32_e32 v65, v186, v66
	v_and_b32_e32 v66, v187, v67
	v_cvt_pk_bf16_f32 v202, v2, v52
	v_cvt_pk_bf16_f32 v203, v53, v54
	v_cvt_pk_bf16_f32 v204, v55, v56
	v_cvt_pk_bf16_f32 v205, v57, v58
	v_cvt_pk_bf16_f32 v206, v59, v60
	v_cvt_pk_bf16_f32 v207, v61, v62
	v_cvt_pk_bf16_f32 v208, v63, v64
	v_cvt_pk_bf16_f32 v209, v65, v66
	v_mfma_f32_32x32x16_bf16 v[52:67], v[202:205], v[100:103], 0
	v_mfma_f32_32x32x16_bf16 v[52:67], v[76:79], v[194:197], v[52:67]
	v_mfma_f32_32x32x16_bf16 v[36:51], v[88:91], v[108:111], v[36:51]
	v_mfma_f32_32x32x16_bf16 v[52:67], v[206:209], v[104:107], v[52:67]
	v_mfma_f32_32x32x16_bf16 v[36:51], v[92:95], v[112:115], v[36:51]
	v_mfma_f32_32x32x16_bf16 v[52:67], v[96:99], v[198:201], v[52:67]
	s_nop 11
	v_add_f32_e32 v2, v67, v51
	v_mov_b32 v2, v2
	s_nop 0
	v_or_b32_e32 v68, s68, v210
	v_lshl_add_u32 v68, v68, 1, v211
	ds_read_b128 v[194:197], v68 offset:17408
	ds_read_b128 v[198:201], v68 offset:8704
	v_add_u32_e32 v68, s69, v222
	v_add_u32_e32 v68, 0x2000, v68
	v_or_b32_e32 v2, s68, v193
	ds_read2_b64 v[202:205], v68 offset0:64 offset1:66
	v_or_b32_e32 v68, s70, v210
	v_mad_u32_u24 v2, v2, s86, v212
	v_lshl_add_u32 v68, v68, 1, v211
	ds_read_b128 v[206:209], v68 offset:17408
	ds_read_b128 v[210:213], v68 offset:8704
	ds_read_b128 v[214:217], v2 offset:26112
	ds_read_b128 v[218:221], v2 offset:26144
	v_add_u32_e32 v2, s71, v222
	v_add_u32_e32 v2, 0x2000, v2
	ds_read2_b64 v[222:225], v2 offset0:64 offset1:66
	v_or_b32_e32 v2, s72, v226
	v_add_u32_e32 v2, s62, v2
	ds_read_b128 v[68:71], v2 offset:41472
	ds_read_b128 v[72:75], v2 offset:41504
	ds_read_b128 v[76:79], v2 offset:44032
	ds_read_b128 v[80:83], v2 offset:44064
	ds_read_b128 v[84:87], v2 offset:41536
	ds_read_b128 v[88:91], v2 offset:41568
	ds_read_b128 v[92:95], v2 offset:44096
	ds_read_b128 v[96:99], v2 offset:44128
	s_waitcnt lgkmcnt(0)
; DI void h_chain(f32x16& S, f32x16& O, HPacks& K, const HOpsK& P, const bf16x8 (&vt)[2], const u32x4 (&vv)[2], int rq, int hh) {
;     f32x16 X;
;     { f32x16 Se;
; #pragma unroll
;       for (int g = 0; g < 4; ++g) {
; #pragma unroll
;           for (int e = 0; e < 4; ++e) Se[4 * g + e] = S[4 * g + e] * P.ebm[g][e]; }
;       K.sp0 = pack_step(Se, 0); K.sp1 = pack_step(Se, 1); }
; #pragma unroll
;     for (int g = 0; g < 4; ++g) {
; #pragma unroll
;         for (int e = 0; e < 4; ++e) S[4 * g + e] *= P.dec[g][e]; }
; #pragma unroll
;     for (int i = 0; i < 16; ++i) { X[i] = 0.f; O[i] = 0.f; }
;     __builtin_amdgcn_sched_barrier(0);
; #pragma unroll
;     for (int st = 0; st < 2; ++st) X = MFMA32(P.ka[st], P.qb[st], X);
; #pragma unroll
;     for (int i = 0; i < 16; ++i) X[i] = (crow(i, hh) <= rq) ? X[i] : 0.f;
;     K.xp0 = pack_step(X, 0); K.xp1 = pack_step(X, 1);
;     __builtin_amdgcn_sched_barrier(0);
;     O = MFMA32(K.xp0, __builtin_bit_cast(bf16x8, vv[0]), O);
;     O = MFMA32(__builtin_bit_cast(bf16x8, P.qq[0]), K.sp0, O);
;     O = MFMA32(K.xp1, __builtin_bit_cast(bf16x8, vv[1]), O);
;     O = MFMA32(__builtin_bit_cast(bf16x8, P.qq[1]), K.sp1, O);
; #pragma unroll
;     for (int st = 0; st < 2; ++st) S = MFMA32(P.ku[st], vt[st], S);
;     __builtin_amdgcn_sched_barrier(0);
; }
; DI void h_mma2(f32x16& S0, f32x16& S1, LAS unsigned char* buf, LAS unsigned char* red, int kbp, int vb, int r32, int hh) {
;     int rq = r32; asm volatile("" : "+v"(rq));
;     bf16x8 vt[2]; u32x4 vv[2];
; #pragma unroll
;     for (int st = 0; st < 2; ++st) {
;         vt[st] = *(const LAS bf16x8*)(buf + H_VT + (vb * 32 + r32) * 80 + (16 * st + 8 * hh) * 2);
;         const LAS unsigned char* vp = buf + H_VT + (vb * 32 + r32) * 80 + (16 * st + 4 * hh) * 2;
;         const u32x2 v0 = *(const LAS u32x2*)vp, v1 = *(const LAS u32x2*)(vp + 16);
;         vv[st].x = v0.x; vv[st].y = v0.y; vv[st].z = v1.x; vv[st].w = v1.y;
;     }
;     f32x16 Osum;
; #pragma unroll
;     for (int kk = 0; kk < 2; ++kk) {
;         HOpsK P; h_opsk_load(P, buf, 2 * kbp + kk, r32, hh);
;         f32x16& S = (kk == 0) ? S0 : S1; f32x16 O;
;         LDS_WAIT(); __builtin_amdgcn_sched_barrier(0);
;         HPacks K;
;         h_chain(S, O, K, P, vt, vv, rq, hh);
;         { float s_ = S[15] + O[15]; asm volatile("v_mov_b32 %0, %0" : "+v"(s_)); asm volatile("" :: "v"(s_)); }
	s_waitcnt lgkmcnt(5)
	v_pk_mul_f32 v[76:77], v[4:5], v[76:77]
	v_pk_mul_f32 v[78:79], v[6:7], v[78:79]
	s_waitcnt lgkmcnt(4)
	v_pk_mul_f32 v[80:81], v[8:9], v[80:81]
	v_pk_mul_f32 v[82:83], v[10:11], v[82:83]
	s_waitcnt lgkmcnt(1)
	v_pk_mul_f32 v[92:93], v[12:13], v[92:93]
	v_pk_mul_f32 v[94:95], v[14:15], v[94:95]
	s_waitcnt lgkmcnt(0)
	v_pk_mul_f32 v[96:97], v[16:17], v[96:97]
	v_pk_mul_f32 v[98:99], v[18:19], v[98:99]
	v_cvt_pk_bf16_f32 v226, v76, v77
	v_cvt_pk_bf16_f32 v227, v78, v79
	v_cvt_pk_bf16_f32 v228, v80, v81
	v_cvt_pk_bf16_f32 v229, v82, v83
	v_pk_mul_f32 v[82:83], v[18:19], v[90:91]
	v_pk_mul_f32 v[78:79], v[14:15], v[86:87]
	v_pk_mul_f32 v[74:75], v[10:11], v[74:75]
	v_pk_mul_f32 v[70:71], v[6:7], v[70:71]
	v_pk_mul_f32 v[80:81], v[16:17], v[88:89]
	v_pk_mul_f32 v[76:77], v[12:13], v[84:85]
	v_pk_mul_f32 v[72:73], v[8:9], v[72:73]
	v_pk_mul_f32 v[68:69], v[4:5], v[68:69]
	v_cvt_pk_bf16_f32 v230, v92, v93
	v_cvt_pk_bf16_f32 v231, v94, v95
	v_cvt_pk_bf16_f32 v232, v96, v97
	v_cvt_pk_bf16_f32 v233, v98, v99
	v_mfma_f32_32x32x16_bf16 v[84:99], v[194:197], v[198:201], 0
	v_mfma_f32_32x32x16_bf16 v[84:99], v[206:209], v[210:213], v[84:99]
	s_nop 11
	v_and_b32_e32 v2, v191, v84
	v_and_b32_e32 v84, v188, v85
	v_and_b32_e32 v85, v189, v86
	v_and_b32_e32 v86, v190, v87
	v_and_b32_e32 v87, v176, v88
	v_and_b32_e32 v88, v177, v89
	v_and_b32_e32 v89, v178, v90
	v_and_b32_e32 v90, v179, v91
	v_and_b32_e32 v91, v180, v92
	v_and_b32_e32 v92, v181, v93
	v_and_b32_e32 v93, v182, v94
	v_and_b32_e32 v94, v183, v95
	v_and_b32_e32 v95, v184, v96
	v_and_b32_e32 v96, v185, v97
	v_and_b32_e32 v97, v186, v98
	v_and_b32_e32 v98, v187, v99
	v_cvt_pk_bf16_f32 v234, v2, v84
	v_cvt_pk_bf16_f32 v235, v85, v86
	v_cvt_pk_bf16_f32 v236, v87, v88
	v_cvt_pk_bf16_f32 v237, v89, v90
	v_cvt_pk_bf16_f32 v238, v91, v92
	v_cvt_pk_bf16_f32 v239, v93, v94
	v_cvt_pk_bf16_f32 v240, v95, v96
	v_cvt_pk_bf16_f32 v241, v97, v98
	v_mfma_f32_32x32x16_bf16 v[84:99], v[234:237], v[100:103], 0
	v_mfma_f32_32x32x16_bf16 v[84:99], v[202:205], v[226:229], v[84:99]
	v_mfma_f32_32x32x16_bf16 v[68:83], v[214:217], v[108:111], v[68:83]
	v_mfma_f32_32x32x16_bf16 v[84:99], v[238:241], v[104:107], v[84:99]
	v_mfma_f32_32x32x16_bf16 v[68:83], v[218:221], v[112:115], v[68:83]
	v_mfma_f32_32x32x16_bf16 v[84:99], v[222:225], v[230:233], v[84:99]
	s_nop 11
	v_add_f32_e32 v2, v99, v83
	v_mov_b32 v2, v2
	s_nop 0
	v_add_f32_e32 v2, v67, v99
	v_add_f32_e32 v66, v66, v98
	v_add_f32_e32 v65, v65, v97
	v_add_f32_e32 v64, v64, v96
	v_add_f32_e32 v63, v63, v95
	v_add_f32_e32 v62, v62, v94
	v_add_f32_e32 v61, v61, v93
	v_add_f32_e32 v60, v60, v92
	v_add_f32_e32 v59, v59, v91
	v_add_f32_e32 v58, v58, v90
	v_add_f32_e32 v57, v57, v89
	v_add_f32_e32 v56, v56, v88
	v_add_f32_e32 v55, v55, v87
	v_add_f32_e32 v54, v54, v86
	v_add_f32_e32 v53, v53, v85
	v_add_f32_e32 v52, v52, v84
	v_add_u32_e32 v67, 0x16800, v242
	ds_write2st64_b32 v67, v52, v53 offset1:1
	ds_write2st64_b32 v67, v54, v55 offset0:2 offset1:3
	ds_write2st64_b32 v67, v56, v57 offset0:8 offset1:9
	ds_write2st64_b32 v67, v58, v59 offset0:10 offset1:11
	ds_write2st64_b32 v67, v60, v61 offset0:16 offset1:17
	ds_write2st64_b32 v67, v62, v63 offset0:18 offset1:19
	ds_write2st64_b32 v67, v64, v65 offset0:24 offset1:25
	ds_write2st64_b32 v67, v66, v2 offset0:26 offset1:27
	s_mov_b64 s[4:5], 0

; #define LAS __attribute__((address_space(3)))
; #define LDS_WAIT() asm volatile("s_waitcnt lgkmcnt(0)" ::: "memory")
; DI int crow(int reg, int h) { return (reg & 3) + 8 * (reg >> 2) + 4 * h; }
; #define HSTEP2(cc, RF, RN, RNN) do { if (prep) h_prep_step<RF, RN, RNN>(CR, A, lds, (cc), rb, h, vhalf); else h_mma_step(S0, S1, lds, (cc), F.wave); __syncthreads(); } while (0)
; DI void h_mma2(f32x16& S0, f32x16& S1, LAS unsigned char* buf, LAS unsigned char* red, int kbp, int vb, int r32, int hh) {
;     int rq = r32; asm volatile("" : "+v"(rq));
;     bf16x8 vt[2]; u32x4 vv[2];
; #pragma unroll
;     for (int st = 0; st < 2; ++st) {
;         vt[st] = *(const LAS bf16x8*)(buf + H_VT + (vb * 32 + r32) * 80 + (16 * st + 8 * hh) * 2);
;         const LAS unsigned char* vp = buf + H_VT + (vb * 32 + r32) * 80 + (16 * st + 4 * hh) * 2;
;         const u32x2 v0 = *(const LAS u32x2*)vp, v1 = *(const LAS u32x2*)(vp + 16);
;         vv[st].x = v0.x; vv[st].y = v0.y; vv[st].z = v1.x; vv[st].w = v1.y;
;     }
;     f32x16 Osum;
; #pragma unroll
;     for (int kk = 0; kk < 2; ++kk) {
;         HOpsK P; h_opsk_load(P, buf, 2 * kbp + kk, r32, hh);
;         f32x16& S = (kk == 0) ? S0 : S1; f32x16 O;
;         LDS_WAIT(); __builtin_amdgcn_sched_barrier(0);
;         HPacks K;
;         h_chain(S, O, K, P, vt, vv, rq, hh);
;         { float s_ = S[15] + O[15]; asm volatile("v_mov_b32 %0, %0" : "+v"(s_)); asm volatile("" :: "v"(s_)); }
;         asm volatile("" :: "v"(P.ka[0]), "v"(P.ka[1]), "v"(P.qb[0]), "v"(P.qb[1]), "v"(P.ku[0]), "v"(P.ku[1]), "v"(P.qq[0]), "v"(P.qq[1]));
;         asm volatile("" :: "v"(K.sp0), "v"(K.sp1), "v"(K.xp0), "v"(K.xp1));
;         __builtin_amdgcn_sched_barrier(0);
; #pragma unroll
;         for (int i = 0; i < 16; ++i) Osum[i] = (kk == 0) ? O[i] : Osum[i] + O[i];
;         __builtin_amdgcn_sched_barrier(0);
;     }
;     asm volatile("" :: "v"(vt[0]), "v"(vt[1]), "v"(vv[0]), "v"(vv[1]));
; #pragma unroll
;     for (int i = 0; i < 16; ++i) *(LAS float*)(red + ((kbp * 32 + crow(i, hh)) * 64 + vb * 32 + r32) * 4) = Osum[i];
; DI void p2_hgrn_roles(Frame& F, ArgsP A) {
;     ...
;         for (int c = 0; c < 63; c += 3) { HSTEP2(c, 0, 1, 2); HSTEP2(c + 1, 1, 2, 0); HSTEP2(c + 2, 2, 0, 1); }
;         HSTEP2(63, 0, 1, 2);
.LBB0_439:
	s_add_i32 s4, s39, 3
	s_add_u32 s56, s56, 0x60000
	s_addc_u32 s57, s57, 0
	s_add_i32 s97, s97, 0x30000
	s_add_i32 s38, s38, 0xc000
	s_cmp_gt_u32 s39, 59
	s_waitcnt lgkmcnt(0)
	s_barrier
	s_cbranch_scc0 .LBB0_412
	s_mov_b64 s[4:5], -1
	s_and_b64 vcc, exec, s[42:43]
	s_cbranch_vccz .LBB0_442
	v_mov_b32_e32 v2, v0
	v_mov_b32_e32 v38, s89
	v_and_b32_e32 v121, 31, v2
	v_bfe_u32 v2, v2, 5, 1
	v_or_b32_e32 v37, s3, v121
	v_mad_u32_u24 v37, v37, s86, v38
	s_waitcnt vmcnt(46)
	v_lshlrev_b32_e32 v128, 4, v2
	s_waitcnt vmcnt(19)
	v_lshlrev_b32_e32 v129, 3, v2
	v_mov_b32_e32 v36, v121
	v_add_u32_e32 v38, v37, v128
	v_add_u32_e32 v37, v37, v129
	ds_read2_b64 v[52:55], v37 offset1:2
	ds_read2_b64 v[56:59], v37 offset0:4 offset1:6
	ds_read_b128 v[60:63], v38
	ds_read_b128 v[64:67], v38 offset:32
	v_lshlrev_b32_e32 v37, 2, v2
	v_mad_u32_u24 v130, v121, s87, 0
	v_or_b32_e32 v37, s63, v129
	s_waitcnt vmcnt(18)
	v_add_u32_e32 v131, v130, v129
	v_lshl_add_u32 v37, v37, 1, v130
	ds_read_b128 v[68:71], v37 offset:63488
	ds_read_b128 v[72:75], v37 offset:54784
	v_add_u32_e32 v37, s64, v131
	v_add_u32_e32 v37, 0xd000, v37
	v_add_u32_e32 v132, s90, v128
	v_or_b32_e32 v36, s63, v121
	ds_read2_b64 v[76:79], v37 offset0:192 offset1:194
	v_or_b32_e32 v37, s65, v129
	v_mad_u32_u24 v36, v36, s86, v132
	v_lshl_add_u32 v37, v37, 1, v130
	ds_read_b128 v[80:83], v37 offset:63488
	ds_read_b128 v[84:87], v37 offset:54784
	ds_read_b128 v[88:91], v36
	ds_read_b128 v[92:95], v36 offset:32
	v_add_u32_e32 v36, s66, v131
	v_add_u32_e32 v36, 0xd000, v36
	v_or_b32_e32 v108, s67, v128
	ds_read2_b64 v[96:99], v36 offset0:192 offset1:194
	v_add_u32_e32 v36, s91, v108
	v_add_u32_e32 v40, s92, v108
	v_or_b32_e32 v44, 32, v108
	v_or_b32_e32 v48, 64, v108
	v_or_b32_e32 v108, 0x60, v108
	v_add_u32_e32 v45, s91, v44
	v_add_u32_e32 v44, s92, v44
	v_add_u32_e32 v49, s91, v48
	v_add_u32_e32 v48, s92, v48
	v_add_u32_e32 v109, s91, v108
	v_add_u32_e32 v112, s92, v108
	ds_read_b128 v[36:39], v36
	ds_read_b128 v[40:43], v40
	ds_read_b128 v[100:103], v45
	ds_read_b128 v[44:47], v44
	ds_read_b128 v[104:107], v49
	ds_read_b128 v[48:51], v48
	ds_read_b128 v[108:111], v109
	ds_read_b128 v[112:115], v112
	s_waitcnt lgkmcnt(0)
	s_waitcnt lgkmcnt(6)
	v_pk_mul_f32 v[40:41], v[20:21], v[40:41]
	v_pk_mul_f32 v[42:43], v[22:23], v[42:43]
	s_waitcnt lgkmcnt(4)
	v_pk_mul_f32 v[44:45], v[24:25], v[44:45]
	v_pk_mul_f32 v[46:47], v[26:27], v[46:47]
	s_waitcnt lgkmcnt(2)
	v_pk_mul_f32 v[48:49], v[28:29], v[48:49]
	v_pk_mul_f32 v[50:51], v[30:31], v[50:51]
	s_waitcnt lgkmcnt(0)
	v_pk_mul_f32 v[116:117], v[32:33], v[112:113]
	v_pk_mul_f32 v[126:127], v[34:35], v[114:115]
	v_cvt_pk_bf16_f32 v112, v40, v41
	v_cvt_pk_bf16_f32 v113, v42, v43
	v_cvt_pk_bf16_f32 v114, v44, v45
	v_cvt_pk_bf16_f32 v115, v46, v47
	v_cvt_pk_bf16_f32 v122, v48, v49
	v_cvt_pk_bf16_f32 v123, v50, v51
	v_cvt_pk_bf16_f32 v124, v116, v117
	v_cvt_pk_bf16_f32 v125, v126, v127
	v_pk_mul_f32 v[38:39], v[22:23], v[38:39]
	v_pk_mul_f32 v[50:51], v[34:35], v[110:111]
	v_pk_mul_f32 v[46:47], v[30:31], v[106:107]
	v_pk_mul_f32 v[42:43], v[26:27], v[102:103]
	v_pk_mul_f32 v[36:37], v[20:21], v[36:37]
	v_pk_mul_f32 v[48:49], v[32:33], v[108:109]
	v_pk_mul_f32 v[44:45], v[28:29], v[104:105]
	v_pk_mul_f32 v[40:41], v[24:25], v[100:101]
	v_mfma_f32_32x32x16_bf16 v[20:35], v[68:71], v[72:75], 0
	v_mfma_f32_32x32x16_bf16 v[20:35], v[80:83], v[84:87], v[20:35]
	s_nop 11
	v_and_b32_e32 v20, v191, v20
	v_and_b32_e32 v21, v188, v21
	v_and_b32_e32 v22, v189, v22
	v_and_b32_e32 v23, v190, v23
	v_and_b32_e32 v24, v176, v24
	v_and_b32_e32 v25, v177, v25
	v_and_b32_e32 v26, v178, v26
	v_and_b32_e32 v27, v179, v27
	v_and_b32_e32 v28, v180, v28
	v_and_b32_e32 v29, v181, v29
	v_and_b32_e32 v30, v182, v30
	v_and_b32_e32 v31, v183, v31
	v_and_b32_e32 v32, v184, v32
	v_and_b32_e32 v33, v185, v33
	v_and_b32_e32 v34, v186, v34
	v_and_b32_e32 v35, v187, v35
	v_cvt_pk_bf16_f32 v100, v20, v21
	v_cvt_pk_bf16_f32 v101, v22, v23
	v_cvt_pk_bf16_f32 v102, v24, v25
	v_cvt_pk_bf16_f32 v103, v26, v27
	v_cvt_pk_bf16_f32 v104, v28, v29
	v_cvt_pk_bf16_f32 v105, v30, v31
	v_cvt_pk_bf16_f32 v106, v32, v33
	v_cvt_pk_bf16_f32 v107, v34, v35
	v_mfma_f32_32x32x16_bf16 v[20:35], v[100:103], v[52:55], 0
	v_mfma_f32_32x32x16_bf16 v[20:35], v[76:79], v[112:115], v[20:35]
	v_mfma_f32_32x32x16_bf16 v[20:35], v[104:107], v[56:59], v[20:35]
	v_mfma_f32_32x32x16_bf16 v[36:51], v[88:91], v[60:63], v[36:51]
	v_mfma_f32_32x32x16_bf16 v[20:35], v[96:99], v[122:125], v[20:35]
	v_mfma_f32_32x32x16_bf16 v[36:51], v[92:95], v[64:67], v[36:51]
	s_nop 11
	v_add_f32_e32 v36, v35, v51
	v_mov_b32 v36, v36
	s_nop 0
	v_or_b32_e32 v37, s68, v129
	v_lshl_add_u32 v37, v37, 1, v130
	ds_read_b128 v[68:71], v37 offset:63488
	ds_read_b128 v[72:75], v37 offset:54784
	v_add_u32_e32 v37, s69, v131
	v_add_u32_e32 v37, 0xd000, v37
	v_or_b32_e32 v36, s68, v121
	ds_read2_b64 v[76:79], v37 offset0:192 offset1:194
	v_or_b32_e32 v37, s70, v129
	v_mad_u32_u24 v36, v36, s86, v132
	v_lshl_add_u32 v37, v37, 1, v130
	ds_read_b128 v[80:83], v37 offset:63488
	ds_read_b128 v[84:87], v37 offset:54784
	ds_read_b128 v[88:91], v36
	ds_read_b128 v[92:95], v36 offset:32
	v_add_u32_e32 v36, s71, v131
	v_add_u32_e32 v36, 0xd000, v36
	v_or_b32_e32 v108, s72, v128
	ds_read2_b64 v[96:99], v36 offset0:192 offset1:194
	v_add_u32_e32 v36, s91, v108
	v_add_u32_e32 v40, s92, v108
	v_or_b32_e32 v44, 32, v108
	v_or_b32_e32 v100, 64, v108
	v_or_b32_e32 v108, 0x60, v108
	v_add_u32_e32 v45, s91, v44
	v_add_u32_e32 v48, s92, v44
	v_add_u32_e32 v101, s91, v100
	v_add_u32_e32 v104, s92, v100
	v_add_u32_e32 v109, s91, v108
	v_add_u32_e32 v112, s92, v108
	ds_read_b128 v[36:39], v36
	ds_read_b128 v[40:43], v40
	ds_read_b128 v[44:47], v45
	ds_read_b128 v[48:51], v48
	ds_read_b128 v[100:103], v101
	ds_read_b128 v[104:107], v104
	ds_read_b128 v[108:111], v109
	ds_read_b128 v[112:115], v112
	s_waitcnt lgkmcnt(0)
; DI void h_chain(f32x16& S, f32x16& O, HPacks& K, const HOpsK& P, const bf16x8 (&vt)[2], const u32x4 (&vv)[2], int rq, int hh) {
;     f32x16 X;
;     { f32x16 Se;
; #pragma unroll
;       for (int g = 0; g < 4; ++g) {
; #pragma unroll
;           for (int e = 0; e < 4; ++e) Se[4 * g + e] = S[4 * g + e] * P.ebm[g][e]; }
;       K.sp0 = pack_step(Se, 0); K.sp1 = pack_step(Se, 1); }
; #pragma unroll
;     for (int g = 0; g < 4; ++g) {
; #pragma unroll
;         for (int e = 0; e < 4; ++e) S[4 * g + e] *= P.dec[g][e]; }
; #pragma unroll
;     for (int i = 0; i < 16; ++i) { X[i] = 0.f; O[i] = 0.f; }
;     __builtin_amdgcn_sched_barrier(0);
; #pragma unroll
;     for (int st = 0; st < 2; ++st) X = MFMA32(P.ka[st], P.qb[st], X);
; #pragma unroll
;     for (int i = 0; i < 16; ++i) X[i] = (crow(i, hh) <= rq) ? X[i] : 0.f;
;     K.xp0 = pack_step(X, 0); K.xp1 = pack_step(X, 1);
;     __builtin_amdgcn_sched_barrier(0);
;     O = MFMA32(K.xp0, __builtin_bit_cast(bf16x8, vv[0]), O);
;     O = MFMA32(__builtin_bit_cast(bf16x8, P.qq[0]), K.sp0, O);
;     O = MFMA32(K.xp1, __builtin_bit_cast(bf16x8, vv[1]), O);
;     O = MFMA32(__builtin_bit_cast(bf16x8, P.qq[1]), K.sp1, O);
; #pragma unroll
;     for (int st = 0; st < 2; ++st) S = MFMA32(P.ku[st], vt[st], S);
;     __builtin_amdgcn_sched_barrier(0);
; }
; DI void h_mma2(f32x16& S0, f32x16& S1, LAS unsigned char* buf, LAS unsigned char* red, int kbp, int vb, int r32, int hh) {
;     int rq = r32; asm volatile("" : "+v"(rq));
;     bf16x8 vt[2]; u32x4 vv[2];
; #pragma unroll
;     for (int st = 0; st < 2; ++st) {
;         vt[st] = *(const LAS bf16x8*)(buf + H_VT + (vb * 32 + r32) * 80 + (16 * st + 8 * hh) * 2);
;         const LAS unsigned char* vp = buf + H_VT + (vb * 32 + r32) * 80 + (16 * st + 4 * hh) * 2;
;         const u32x2 v0 = *(const LAS u32x2*)vp, v1 = *(const LAS u32x2*)(vp + 16);
;         vv[st].x = v0.x; vv[st].y = v0.y; vv[st].z = v1.x; vv[st].w = v1.y;
;     }
;     f32x16 Osum;
; #pragma unroll
;     for (int kk = 0; kk < 2; ++kk) {
;         HOpsK P; h_opsk_load(P, buf, 2 * kbp + kk, r32, hh);
;         f32x16& S = (kk == 0) ? S0 : S1; f32x16 O;
;         LDS_WAIT(); __builtin_amdgcn_sched_barrier(0);
;         HPacks K;
;         h_chain(S, O, K, P, vt, vv, rq, hh);
;         { float s_ = S[15] + O[15]; asm volatile("v_mov_b32 %0, %0" : "+v"(s_)); asm volatile("" :: "v"(s_)); }
	s_waitcnt lgkmcnt(6)
	v_pk_mul_f32 v[40:41], v[4:5], v[40:41]
	v_pk_mul_f32 v[42:43], v[6:7], v[42:43]
	s_waitcnt lgkmcnt(4)
	v_pk_mul_f32 v[48:49], v[8:9], v[48:49]
	v_pk_mul_f32 v[50:51], v[10:11], v[50:51]
	s_waitcnt lgkmcnt(2)
	v_pk_mul_f32 v[116:117], v[12:13], v[104:105]
	v_pk_mul_f32 v[122:123], v[14:15], v[106:107]
	s_waitcnt lgkmcnt(0)
	v_pk_mul_f32 v[124:125], v[16:17], v[112:113]
	v_pk_mul_f32 v[126:127], v[18:19], v[114:115]
	v_cvt_pk_bf16_f32 v104, v40, v41
	v_cvt_pk_bf16_f32 v105, v42, v43
	v_cvt_pk_bf16_f32 v106, v48, v49
	v_cvt_pk_bf16_f32 v107, v50, v51
	v_cvt_pk_bf16_f32 v112, v116, v117
	v_cvt_pk_bf16_f32 v113, v122, v123
	v_cvt_pk_bf16_f32 v114, v124, v125
	v_cvt_pk_bf16_f32 v115, v126, v127
	v_pk_mul_f32 v[18:19], v[18:19], v[110:111]
	v_pk_mul_f32 v[14:15], v[14:15], v[102:103]
	v_pk_mul_f32 v[10:11], v[10:11], v[46:47]
	v_pk_mul_f32 v[6:7], v[6:7], v[38:39]
	v_pk_mul_f32 v[16:17], v[16:17], v[108:109]
	v_pk_mul_f32 v[12:13], v[12:13], v[100:101]
	v_pk_mul_f32 v[8:9], v[8:9], v[44:45]
	v_pk_mul_f32 v[4:5], v[4:5], v[36:37]
	v_mfma_f32_32x32x16_bf16 v[36:51], v[68:71], v[72:75], 0
	v_mfma_f32_32x32x16_bf16 v[36:51], v[80:83], v[84:87], v[36:51]
	s_nop 11
	v_and_b32_e32 v36, v191, v36
	v_and_b32_e32 v37, v188, v37
	v_and_b32_e32 v38, v189, v38
	v_and_b32_e32 v39, v190, v39
	v_and_b32_e32 v40, v176, v40
	v_and_b32_e32 v41, v177, v41
	v_and_b32_e32 v42, v178, v42
	v_and_b32_e32 v43, v179, v43
	v_and_b32_e32 v44, v180, v44
	v_and_b32_e32 v45, v181, v45
	v_and_b32_e32 v46, v182, v46
	v_and_b32_e32 v47, v183, v47
	v_and_b32_e32 v48, v184, v48
	v_and_b32_e32 v49, v185, v49
	v_and_b32_e32 v50, v186, v50
	v_and_b32_e32 v51, v187, v51
	v_cvt_pk_bf16_f32 v100, v36, v37
	v_cvt_pk_bf16_f32 v101, v38, v39
	v_cvt_pk_bf16_f32 v102, v40, v41
	v_cvt_pk_bf16_f32 v103, v42, v43
	v_cvt_pk_bf16_f32 v108, v44, v45
	v_cvt_pk_bf16_f32 v109, v46, v47
	v_cvt_pk_bf16_f32 v110, v48, v49
	v_cvt_pk_bf16_f32 v111, v50, v51
	v_mfma_f32_32x32x16_bf16 v[36:51], v[100:103], v[52:55], 0
	v_mfma_f32_32x32x16_bf16 v[36:51], v[76:79], v[104:107], v[36:51]
	v_mfma_f32_32x32x16_bf16 v[36:51], v[108:111], v[56:59], v[36:51]
	v_mfma_f32_32x32x16_bf16 v[4:19], v[88:91], v[60:63], v[4:19]
	v_mfma_f32_32x32x16_bf16 v[36:51], v[96:99], v[112:115], v[36:51]
	v_mfma_f32_32x32x16_bf16 v[4:19], v[92:95], v[64:67], v[4:19]
	s_nop 11
	v_add_f32_e32 v4, v51, v19
	v_mov_b32 v4, v4
	s_nop 0
	v_add_f32_e32 v4, v35, v51
	v_add_f32_e32 v5, v34, v50
	v_add_f32_e32 v6, v33, v49
	v_add_f32_e32 v7, v32, v48
	v_add_f32_e32 v8, v31, v47
	v_add_f32_e32 v9, v30, v46
	v_add_f32_e32 v10, v29, v45
	v_add_f32_e32 v11, v28, v44
	v_add_f32_e32 v12, v27, v43
	v_add_f32_e32 v13, v26, v42
	v_add_f32_e32 v14, v25, v41
	v_add_f32_e32 v15, v24, v40
	v_add_f32_e32 v16, v23, v39
	v_add_f32_e32 v17, v22, v38
	v_add_f32_e32 v18, v21, v37
	v_add_f32_e32 v19, v20, v36
	v_lshlrev_b32_e32 v2, 8, v2
	v_or3_b32 v2, v2, s73, v121
	v_lshl_add_u32 v2, v2, 2, 0
	v_add_u32_e32 v2, 0x1a800, v2
	ds_write2st64_b32 v2, v19, v18 offset1:1
	ds_write2st64_b32 v2, v17, v16 offset0:2 offset1:3
	ds_write2st64_b32 v2, v15, v14 offset0:8 offset1:9
	ds_write2st64_b32 v2, v13, v12 offset0:10 offset1:11
	ds_write2st64_b32 v2, v11, v10 offset0:16 offset1:17
	ds_write2st64_b32 v2, v9, v8 offset0:18 offset1:19
	ds_write2st64_b32 v2, v7, v6 offset0:24 offset1:25
	ds_write2st64_b32 v2, v5, v4 offset0:26 offset1:27
	s_mov_b64 s[4:5], 0
